# speedup vs baseline: 1.0104x; 1.0104x over previous
.LBB1_2:
	s_or_b64 exec, exec, s[2:3]
	v_and_b32_e32 v52, 3, v52
	v_and_b32_e32 v54, 48, v0
	v_lshlrev_b32_e32 v55, 2, v0
	v_lshl_or_b32 v54, v50, 6, v54
	v_and_b32_e32 v55, 32, v55
	v_lshlrev_b32_e32 v56, 14, v53
	v_lshlrev_b32_e32 v57, 13, v52
	v_lshl_or_b32 v52, v52, 6, s20
	v_lshlrev_b32_e32 v51, 2, v51
	s_movk_i32 s2, 0x4c
	v_bitop3_b32 v191, v54, v57, v55 bitop3:0xde
	v_bitop3_b32 v192, v54, v56, v55 bitop3:0xde
	v_or_b32_e32 v54, v52, v51
	v_bitop3_b32 v51, v52, s2, v51 bitop3:0xc8
	v_lshrrev_b32_e32 v52, 6, v52
	s_lshl_b32 s2, s19, 2
	v_and_or_b32 v52, v52, 14, s18
	v_lshlrev_b32_e32 v182, 2, v51
	v_mov_b32_e32 v183, 0
	s_add_u32 s2, s8, s2
	v_lshlrev_b32_e32 v52, 14, v52
	v_lshlrev_b32_e32 v53, 7, v53
	v_lshl_add_u64 v[184:185], s[10:11], 0, v[182:183]
	s_addc_u32 s3, s9, 0
	v_lshlrev_b32_e32 v182, 2, v54
	v_or3_b32 v193, v53, v52, v50
	s_mov_b32 s18, 0
	v_lshl_add_u64 v[186:187], s[2:3], 0, v[182:183]
	s_mov_b32 s2, s6
	s_mov_b32 s3, s7
	s_movk_i32 s8, 0x2000
	s_movk_i32 s9, 0x6000
	s_mov_b32 s10, 0xa000
	s_mov_b32 s11, 0xe000
	s_mov_b32 s19, 0
	s_mov_b32 s20, 0
	s_branch .Lfirst
	.p2align	6
